# GDN in-proj rounds 1-3: XCD keeps 4 weight column tiles x 8 row tiles per round (weights stay in its L2); plus the XCD-aware MoE-up map (variant b)
# speedup vs baseline: 1.0007x; 1.0007x over previous
;     __device__ __forceinline__ bool next(int i, pg8::Unit& u) const { if (i > 0) return false; u.pm = pm; u.pn = pn; u.e = 0; u.mt = 0; u.cnt = 0; u.lx = 0; u.a = A + ((size_t)pm * 256 + rowoff) * 2048; u.b = Bt + (size_t)pn * 256 * 2048; return true; }
;     __device__ __forceinline__ bool next(int i, pg8::Unit& u) const {
;         const int Lx = i * G + c; if (Lx >= total) return false;
;         const int grp = Lx / (8 * nN), r = Lx % (8 * nN);
;         const int j = grp * 8 + (r & 7); u.pm = latent_only ? (j >> 3) * 9 + 1 + (j & 7) : j; u.pn = r >> 3; u.e = 0; u.mt = 0; u.cnt = 0; u.lx = Lx;
;         u.a = A + (size_t)u.pm * 256 * 2048; u.b = Bt + (size_t)u.pn * 256 * 2048;
;         return true;
;     }
.LBB0_555:
	s_add_i32 s30, s30, 1
	s_mul_i32 s15, s30, s88
	s_add_i32 s15, s15, s86
	s_cmpk_lt_i32 s15, 0x480
	s_cselect_b64 s[42:43], -1, 0
	s_cmpk_gt_i32 s15, 0x47f
	s_cbranch_scc1 .LBB0_557
	s_cmpk_lt_i32 s15, 0x400
	s_cbranch_scc0 .Lgin_map_old
	s_cmp_lg_u32 s88, 0x100
	s_cbranch_scc1 .Lgin_map_old
	s_bfe_u32 s14, s86, 0x10002
	s_lshl_b32 s14, s14, 3
	s_bfe_u32 s16, s86, 0x30005
	s_or_b32 s14, s14, s16
	s_lshl_b32 s16, s30, 4
	s_add_i32 s14, s14, s16
	s_and_b32 s16, s86, 3
	s_lshl_b32 s16, s16, 2
	s_bfe_u32 s72, s86, 0x20003
	s_or_b32 s16, s16, s72
	s_branch .Lgin_map_done
.Lgin_map_old:
	s_ashr_i32 s14, s15, 31
	s_lshr_b32 s14, s14, 25
	s_add_i32 s14, s15, s14
	s_ashr_i32 s16, s14, 7
	s_and_b32 s14, s14, 0xffffff80
	s_sub_i32 s15, s15, s14
	s_and_b32 s14, s15, 7
	s_lshl_b32 s16, s16, 3
	s_or_b32 s14, s14, s16
	s_ashr_i32 s16, s15, 3
.Lgin_map_done:
	s_ashr_i32 s15, s14, 31
	s_lshl_b64 s[38:39], s[14:15], 19
	s_add_u32 s38, s78, s38
	s_addc_u32 s39, s79, s39
	s_ashr_i32 s17, s16, 31
	s_lshl_b64 s[40:41], s[16:17], 19
	v_readlane_b32 s15, v252, 60
	s_add_u32 s40, s15, s40
	v_readlane_b32 s15, v252, 61
	s_addc_u32 s41, s15, s41
